# GLA seq pass split into 64 quarter-channel items: waves 0-3 compute, waves 4-7 only stage operands
# speedup vs baseline: 1.0318x; 1.0069x over previous
.LBB0_667:
	s_cmp_lt_i32 s40, 5
	s_cselect_b64 s[4:5], -1, 0
	s_and_b64 s[20:21], s[4:5], s[2:3]
	s_andn2_b64 vcc, exec, s[20:21]
	s_cbranch_vccnz .LBB0_718
	s_waitcnt lgkmcnt(0)
	v_mbcnt_lo_u32_b32 v1, -1, 0
	v_mbcnt_hi_u32_b32 v1, -1, v1
	s_cmp_gt_i32 s24, 63
	v_or_b32_e32 v0, s25, v1
	s_mov_b64 s[2:3], s[0:1]
	v_readfirstlane_b32 s4, v0
	s_cbranch_scc1 .LBB0_690
	s_load_dwordx2 s[6:7], s[2:3], 0xb8
	s_load_dword s16, s[0:1], 0xc8
	s_movk_i32 s8, 0x110
	v_ashrrev_i32_e32 v12, 3, v0
	v_and_b32_e32 v8, 15, v1
	s_waitcnt lgkmcnt(0)
	s_add_u32 s17, s6, 0x8800000
	s_addc_u32 s18, s7, 0
	s_ashr_i32 s2, s4, 2
	v_bfi_b32 v10, -16, s2, v1
	v_mul_lo_u32 v2, v10, s8
	v_add_u32_e32 v132, 0, v2
	v_lshlrev_b32_e32 v2, 6, v12
	v_bfe_u32 v9, v1, 4, 2
	v_ashrrev_i32_e32 v3, 31, v2
	v_lshlrev_b32_e32 v1, 4, v1
	v_mov_b32_e32 v105, 0
	v_lshl_add_u64 v[2:3], v[2:3], 1, s[6:7]
	v_and_b32_e32 v4, 0x70, v1
	v_mov_b32_e32 v5, v105
	v_lshlrev_b32_e32 v133, 4, v0
	s_and_b32 s4, s2, -16
	v_lshl_add_u64 v[2:3], v[2:3], 0, v[4:5]
	s_mov_b64 s[2:3], 0x4000000
	v_and_b32_e32 v104, 0xf0, v133
	v_lshl_add_u64 v[106:107], v[2:3], 0, s[2:3]
	v_lshl_add_u64 v[2:3], s[6:7], 0, v[104:105]
	s_mov_b64 s[2:3], 0x4800000
	v_lshl_add_u64 v[108:109], v[2:3], 0, s[2:3]
	v_and_b32_e32 v2, 0x70, v133
	v_mov_b32_e32 v3, v105
	v_lshl_add_u64 v[6:7], s[6:7], 0, v[2:3]
	s_mov_b64 s[2:3], 0x5800000
	v_lshl_add_u64 v[110:111], v[6:7], 0, s[2:3]
	s_mov_b64 s[2:3], 0x6800000
	v_lshl_add_u64 v[112:113], v[6:7], 0, s[2:3]
	v_lshlrev_b32_e32 v6, 2, v0
	v_lshlrev_b32_e32 v1, 3, v0
	v_ashrrev_i32_e32 v7, 31, v6
	v_lshl_add_u64 v[6:7], v[6:7], 2, s[6:7]
	s_mov_b64 s[6:7], 0x3c00000
	v_and_b32_e32 v116, 0xffffff80, v1
	v_and_b32_e32 v118, 0xffffffc0, v1
	v_add_u32_e32 v1, 0x200, v0
	v_lshl_add_u64 v[114:115], v[6:7], 0, s[6:7]
	s_movk_i32 s6, 0x90
	v_add_u32_e32 v135, 0, v2
	v_lshlrev_b32_e32 v2, 7, v10
	v_lshlrev_b32_e32 v7, 3, v1
	v_lshlrev_b32_e32 v11, 3, v9
	v_cmp_gt_i32_e64 s[2:3], 32, v0
	v_mul_lo_u32 v134, v12, s6
	v_lshlrev_b32_e32 v136, 4, v9
	v_sub_u32_e32 v6, v132, v2
	v_lshlrev_b32_e32 v2, 2, v9
	v_and_b32_e32 v120, 0xffffff80, v7
	v_and_b32_e32 v122, 0xffffffc0, v7
	v_lshrrev_b32_e32 v0, 4, v0
	v_lshrrev_b32_e32 v7, 4, v1
	v_lshrrev_b32_e32 v1, 3, v1
	v_add_u32_e32 v3, 0, v134
	v_add_u32_e32 v5, 0, v104
	v_add_u32_e32 v137, 0, v136
	s_ashr_i32 s5, s4, 31
	v_mul_lo_u32 v0, v0, s8
	v_mul_lo_u32 v7, v7, s8
	v_mul_lo_u32 v1, v1, s6
	v_mad_u32_u24 v9, v8, s6, 0
	v_mul_u32_u24_e32 v10, 0x110, v8
	v_lshlrev_b32_e32 v104, 1, v2
	v_add_u32_e32 v2, v132, v11
	v_ashrrev_i32_e32 v117, 31, v116
	v_ashrrev_i32_e32 v119, 31, v118
	v_ashrrev_i32_e32 v121, 31, v120
	v_ashrrev_i32_e32 v123, 31, v122
	v_or_b32_e32 v138, 0x70, v8
	s_lshl_b32 s19, s24, 8
	s_lshl_b32 s22, s16, 8
	s_lshl_b64 s[4:5], s[4:5], 1
	v_add_u32_e32 v139, 0xf800, v2
	v_add_u32_e32 v140, v3, v4
	v_add_u32_e32 v141, v5, v0
	v_add_u32_e32 v142, v5, v7
	v_add_u32_e32 v143, v135, v1
	v_add_u32_e32 v144, v6, v136
	v_add_u32_e32 v145, v9, v136
	v_add_u32_e32 v146, v137, v10
	s_mov_b32 s23, s24
	s_branch .LBB0_671
.LBB0_670:
	s_add_i32 s23, s23, s16
	s_add_i32 s19, s19, s22
	s_cmp_gt_i32 s23, 63
	s_cbranch_scc1 .LBB0_690
.LBB0_671:
	s_ashr_i32 s8, s23, 2
	s_ashr_i32 s9, s8, 31
	s_and_b32 s14, s23, 3
	s_lshl_b64 s[6:7], s[8:9], 19
	s_waitcnt vmcnt(0)
	v_lshl_add_u64 v[16:17], v[106:107], 0, s[6:7]
	s_lshl_b64 s[6:7], s[8:9], 20
	s_lshl_b32 s10, s14, 12
	v_lshl_add_u64 v[24:25], v[108:109], 0, s[6:7]
	v_lshl_add_u64 v[26:27], v[110:111], 0, s[6:7]
	s_lshl_b64 s[6:7], s[8:9], 21
	v_add_u32_e32 v124, s10, v118
	v_add_u32_e32 v126, s10, v122
	v_lshl_add_u64 v[32:33], v[112:113], 0, s[6:7]
	v_ashrrev_i32_e32 v125, 31, v124
	v_ashrrev_i32_e32 v127, 31, v126
	v_lshl_add_u64 v[18:19], v[116:117], 1, v[24:25]
	v_lshl_add_u64 v[28:29], v[118:119], 1, v[26:27]
	v_lshl_add_u64 v[30:31], v[124:125], 1, v[32:33]
	v_lshl_add_u64 v[34:35], v[120:121], 1, v[24:25]
	v_lshl_add_u64 v[32:33], v[126:127], 1, v[32:33]
	v_mov_b32 v36, 0
	v_mov_b32 v37, 0
	global_load_dwordx4 v[8:11], v[16:17], off
	global_load_dwordx4 v[12:15], v[18:19], off
	s_nop 0
	global_load_dwordx4 v[16:19], v[28:29], off
	global_load_dwordx4 v[20:23], v[30:31], off
	v_lshl_add_u64 v[38:39], v[122:123], 1, v[26:27]
	global_load_dwordx4 v[24:27], v[34:35], off
	global_load_dwordx4 v[28:31], v[38:39], off
	s_nop 0
	global_load_dwordx4 v[32:35], v[32:33], off
	ds_write2_b64 v139, v[36:37], v[36:37] offset1:4
	ds_write2_b64 v139, v[36:37], v[36:37] offset0:8 offset1:12
	ds_write2_b64 v139, v[36:37], v[36:37] offset0:16 offset1:20
	ds_write2_b64 v139, v[36:37], v[36:37] offset0:24 offset1:28
	s_and_saveexec_b64 s[6:7], s[2:3]
	s_cbranch_execz .LBB0_673
	s_lshl_b64 s[10:11], s[8:9], 15
	v_lshl_add_u64 v[4:5], v[114:115], 0, s[10:11]
	global_load_dwordx4 v[4:7], v[4:5], off

.LBB0_677:
	s_or_b64 exec, exec, s[12:13]
	s_lshl_b32 s8, s8, 9
	s_and_b32 s9, s19, 0xfffff000
	s_and_b32 s8, s8, 0x600
	s_add_u32 s8, s17, s8
	v_or_b32_e32 v128, s9, v138
	s_addc_u32 s9, s18, 0
	s_lshl_b32 s10, s14, 7
	s_add_u32 s8, s8, s10
	s_addc_u32 s9, s9, 0
	s_add_u32 s8, s8, s4
	s_addc_u32 s9, s9, s5
	v_mov_b32_e32 v64, 0
	v_lshl_add_u64 v[130:131], s[8:9], 0, v[104:105]
	s_mov_b32 s27, 0
	v_mov_b32_e32 v65, v64
	v_mov_b32_e32 v66, v64
	v_mov_b32_e32 v67, v64
	v_mov_b32_e32 v68, v64
	v_mov_b32_e32 v69, v64
	v_mov_b32_e32 v70, v64
	v_mov_b32_e32 v71, v64
	v_mov_b32_e32 v72, v64
	v_mov_b32_e32 v73, v64
	v_mov_b32_e32 v74, v64
	v_mov_b32_e32 v75, v64
	v_mov_b32_e32 v92, v64
	v_mov_b32_e32 v93, v64
	v_mov_b32_e32 v94, v64
	v_mov_b32_e32 v95, v64
	v_mov_b32_e32 v84, v64
	v_mov_b32_e32 v85, v64
	v_mov_b32_e32 v86, v64
	v_mov_b32_e32 v87, v64
	v_mov_b32_e32 v88, v64
	v_mov_b32_e32 v89, v64
	v_mov_b32_e32 v90, v64
	v_mov_b32_e32 v91, v64
	v_mov_b32_e32 v76, v64
	v_mov_b32_e32 v77, v64
	v_mov_b32_e32 v78, v64
	v_mov_b32_e32 v79, v64
	v_mov_b32_e32 v80, v64
	v_mov_b32_e32 v81, v64
	v_mov_b32_e32 v82, v64
	v_mov_b32_e32 v83, v64
	s_cmp_ge_u32 s25, 0x100
	s_cbranch_scc1 .Lsq_helper

.Lsq_helper:
.Lsq_h_loop:
	s_add_i32 s26, s27, 2
	s_cmp_lt_u32 s27, 62
	s_cselect_b32 s12, s26, s27
	s_add_u32 s12, s6, s12
	s_addc_u32 s13, s7, 0
	s_lshl_b64 s[14:15], s[12:13], 13
	v_lshl_add_u64 v[64:65], v[106:107], 0, s[14:15]
	s_lshl_b64 s[14:15], s[12:13], 14
	v_lshl_add_u64 v[66:67], v[108:109], 0, s[14:15]
	v_lshl_add_u64 v[68:69], v[110:111], 0, s[14:15]
	s_lshl_b64 s[14:15], s[12:13], 15
	v_lshl_add_u64 v[70:71], v[112:113], 0, s[14:15]
	v_lshl_add_u64 v[72:73], v[116:117], 1, v[66:67]
	v_lshl_add_u64 v[74:75], v[118:119], 1, v[68:69]
	v_lshl_add_u64 v[76:77], v[124:125], 1, v[70:71]
	v_lshl_add_u64 v[78:79], v[120:121], 1, v[66:67]
	v_lshl_add_u64 v[80:81], v[122:123], 1, v[68:69]
	global_load_dwordx4 v[36:39], v[64:65], off
	global_load_dwordx4 v[40:43], v[72:73], off
	global_load_dwordx4 v[44:47], v[74:75], off
	global_load_dwordx4 v[48:51], v[76:77], off
	global_load_dwordx4 v[52:55], v[78:79], off
	global_load_dwordx4 v[56:59], v[80:81], off
	s_barrier
	s_waitcnt vmcnt(6)
	ds_write_b128 v140, v[8:11]
	ds_write_b128 v141, v[12:15] offset:9216
	ds_write_b128 v147, v[16:19] offset:26624
	ds_write_b128 v147, v[20:23] offset:45056
	ds_write_b128 v142, v[24:27] offset:9216
	ds_write_b128 v143, v[28:31] offset:26624
	s_waitcnt lgkmcnt(0)
	s_barrier
	s_cmp_lt_u32 s27, 61
	s_cselect_b32 s12, 3, 1
	s_add_i32 s12, s27, s12
	s_add_u32 s12, s6, s12
	s_addc_u32 s13, s7, 0
	s_lshl_b64 s[14:15], s[12:13], 13
	v_lshl_add_u64 v[64:65], v[106:107], 0, s[14:15]
	s_lshl_b64 s[14:15], s[12:13], 14
	v_lshl_add_u64 v[66:67], v[108:109], 0, s[14:15]
	v_lshl_add_u64 v[68:69], v[110:111], 0, s[14:15]
	s_lshl_b64 s[14:15], s[12:13], 15
	v_lshl_add_u64 v[70:71], v[112:113], 0, s[14:15]
	v_lshl_add_u64 v[72:73], v[116:117], 1, v[66:67]
	v_lshl_add_u64 v[74:75], v[118:119], 1, v[68:69]
	v_lshl_add_u64 v[76:77], v[124:125], 1, v[70:71]
	v_lshl_add_u64 v[78:79], v[120:121], 1, v[66:67]
	v_lshl_add_u64 v[80:81], v[122:123], 1, v[68:69]
	global_load_dwordx4 v[8:11], v[64:65], off
	global_load_dwordx4 v[12:15], v[72:73], off
	global_load_dwordx4 v[16:19], v[74:75], off
	global_load_dwordx4 v[20:23], v[76:77], off
	global_load_dwordx4 v[24:27], v[78:79], off
	global_load_dwordx4 v[28:31], v[80:81], off
	s_barrier
	s_cmp_gt_u32 s27, 61
	s_cbranch_scc1 .Lsq_h_last
	s_waitcnt vmcnt(6)
	ds_write_b128 v140, v[36:39]
	ds_write_b128 v141, v[40:43] offset:9216
	ds_write_b128 v147, v[44:47] offset:26624
	ds_write_b128 v147, v[48:51] offset:45056
	ds_write_b128 v142, v[52:55] offset:9216
	ds_write_b128 v143, v[56:59] offset:26624
.Lsq_h_last:
	s_waitcnt lgkmcnt(0)
	s_barrier
	s_cmp_gt_u32 s27, 61
	s_cbranch_scc1 .LBB0_670
	s_mov_b32 s27, s26
	s_branch .Lsq_h_loop
